# speedup vs baseline: 1.0360x; 1.0049x over previous
.Lattn_prio_done:
	s_lshl_b32 s52, s13, 4
	s_lshl_b32 s0, s2, 12
	v_and_b32_e32 v56, 15, v0
	v_bfe_u32 v15, v0, 4, 2
	v_lshrrev_b32_e32 v14, 1, v0
	v_bfe_u32 v2, v0, 1, 3
	s_add_i32 s54, s52, s0
	v_lshlrev_b32_e32 v16, 7, v56
	v_bitop3_b32 v3, v15, v14, 7 bitop3:0x78
	v_bitop3_b32 v2, v15, v2, 4 bitop3:0x36
	s_bfe_u32 s53, s12, 0x50002
	v_or_b32_e32 v18, s54, v56
	v_lshl_or_b32 v57, v3, 4, v16
	v_lshl_or_b32 v81, v2, 4, v16
	v_lshl_add_u32 v2, s53, 7, v18
	v_mov_b32_e32 v3, v51
	v_lshlrev_b64 v[2:3], 7, v[2:3]
	v_and_b32_e32 v50, 48, v0
	s_waitcnt lgkmcnt(0)
	v_lshl_add_u64 v[2:3], s[14:15], 0, v[2:3]
	v_lshl_add_u64 v[12:13], v[2:3], 0, v[50:51]
	global_load_dwordx4 v[2:5], v[12:13], off offset:64
	global_load_dwordx4 v[6:9], v[12:13], off
	v_and_b32_e32 v11, 63, v0
	v_bfe_u32 v12, v0, 5, 1
	s_mulk_i32 s13, 0xc00
	v_and_b32_e32 v13, 7, v0
	v_cmp_gt_u32_e64 s[0:1], 16, v11
	v_bitop3_b32 v11, v12, v0, 7 bitop3:0x78
	s_lshr_b32 s55, s3, 8
	s_add_i32 s3, s50, s13
	v_and_b32_e32 v14, 8, v14
	v_lshlrev_b32_e32 v23, 4, v11
	v_bitop3_b32 v11, v12, v13, 2 bitop3:0x36
	v_add3_u32 v19, s3, v16, v14
	v_bfe_u32 v14, v0, 3, 3
	v_lshlrev_b32_e32 v24, 4, v11
	v_bitop3_b32 v11, v12, v13, 4 bitop3:0x36
	v_bitop3_b32 v16, v14, v0, 7 bitop3:0x78
	v_lshlrev_b32_e32 v25, 4, v11
	v_bitop3_b32 v11, v12, v13, 6 bitop3:0x36
	v_bitop3_b32 v0, v15, v0, 15 bitop3:0x78
	v_lshl_add_u64 v[58:59], s[14:15], 0, v[50:51]
	v_lshlrev_b32_e32 v50, 4, v13
	v_lshlrev_b32_e32 v13, 4, v11
	v_or_b32_e32 v11, 8, v14
	v_lshlrev_b32_e32 v86, 4, v0
	v_bitop3_b32 v0, v15, v56, 4 bitop3:0x36
	v_or_b32_e32 v17, 4, v15
	v_lshl_add_u32 v21, v16, 4, s3
	v_lshlrev_b32_e32 v26, 7, v14
	v_lshlrev_b32_e32 v12, 6, v14
	v_lshlrev_b32_e32 v27, 7, v11
	v_lshlrev_b32_e32 v14, 6, v11
	v_lshlrev_b32_e32 v87, 4, v0
	v_or_b32_e32 v0, 8, v15
	v_bitop3_b32 v11, v15, v56, 8 bitop3:0x36
	v_bitop3_b32 v16, v15, v56, 12 bitop3:0x36
	v_lshlrev_b32_e32 v83, 2, v15
	v_add_u32_e32 v84, 0x80, v18
	v_lshl_add_u64 v[60:61], s[10:11], 0, v[50:51]
	v_lshlrev_b32_e32 v50, 4, v56
	v_lshlrev_b32_e32 v88, 4, v11
	v_or_b32_e32 v11, 12, v15
	v_lshlrev_b32_e32 v89, 4, v16
	v_lshl_add_u32 v28, v15, 8, s3
	v_lshlrev_b32_e32 v16, 6, v15
	v_lshl_add_u32 v15, v17, 8, s3
	v_lshlrev_b32_e32 v18, 6, v17
	v_lshl_add_u32 v17, v0, 8, s3
	v_lshlrev_b32_e32 v20, 6, v0
	v_add_u32_e32 v0, v1, v10
	v_lshl_add_u64 v[62:63], s[8:9], 0, v[50:51]
	s_lshl_b32 s8, s53, 1
	v_lshl_or_b32 v50, s2, 19, v0
	s_mov_b64 s[46:47], 0x2000
	v_lshl_add_u32 v85, v56, 8, s3
	v_lshl_add_u32 v29, v11, 8, s3
	v_lshlrev_b32_e32 v22, 6, v11
	s_add_i32 s3, s55, s8
	v_lshl_add_u64 v[10:11], v[50:51], 0, s[46:47]
	v_or_b32_e32 v82, s52, v56
	s_add_i32 s56, s8, 2
	s_sub_i32 s57, 0, s3
	v_lshl_add_u64 v[0:1], s[4:5], 0, v[10:11]
	v_mov_b32_e32 v64, v50
	s_mov_b32 s58, 0x40c00000
	s_mov_b32 s36, 0x3c003c00
	v_mov_b32_e32 v116, s36
	v_mov_b32_e32 v117, s36
	v_mov_b32_e32 v118, s36
	v_mov_b32_e32 v119, s36
	v_add_u32_e32 v90, v19, v23
	v_add_u32_e32 v91, v19, v24
	v_add_u32_e32 v92, v19, v25
	v_add_u32_e32 v93, v19, v13
	v_add_u32_e32 v94, v21, v26
	v_lshlrev_b32_e32 v50, 1, v12
	v_add_u32_e32 v95, v21, v27
	v_lshlrev_b32_e32 v66, 1, v14
	v_add_u32_e32 v96, v28, v86
	v_lshlrev_b32_e32 v68, 2, v16
	v_add_u32_e32 v97, v15, v87
	v_lshlrev_b32_e32 v70, 2, v18
	v_add_u32_e32 v98, v17, v88
	v_lshlrev_b32_e32 v72, 2, v20
	v_add_u32_e32 v99, v29, v89
	v_lshlrev_b32_e32 v74, 2, v22
	v_mov_b32_e32 v100, 0xff800000
	v_mov_b32_e32 v101, 0xf149f2ca
	s_mov_b32 s59, s41
	s_branch .LBB2_3

.LBB2_5:
	v_exp_f32_e32 v69, v46
	v_exp_f32_e32 v71, v47
	v_exp_f32_e32 v80, v42
	v_exp_f32_e32 v102, v43
	v_exp_f32_e32 v46, v44
	v_exp_f32_e32 v47, v45
	ds_read_b128 v[42:45], v114 offset:8192
	v_exp_f32_e32 v73, v48
	v_exp_f32_e32 v75, v49
	v_cvt_pk_f16_f32 v79, v46, v47
	v_cvt_pk_f16_f32 v78, v80, v102
	v_cvt_pk_f16_f32 v77, v73, v75
	v_cvt_pk_f16_f32 v76, v69, v71
	ds_read_b128 v[46:49], v114 offset:10240
	ds_read_b128 v[102:105], v114 offset:12288
	s_waitcnt lgkmcnt(0)
	v_mfma_f32_16x16x32_f16 v[26:29], v[42:45], v[76:79], v[26:29]
	ds_read_b128 v[42:45], v114 offset:14336
	v_exp_f32_e32 v106, v38
	v_exp_f32_e32 v107, v39
	v_mfma_f32_16x16x32_f16 v[22:25], v[46:49], v[76:79], v[22:25]
	ds_read_b128 v[46:49], v115 offset:8192
	v_exp_f32_e32 v109, v40
	v_exp_f32_e32 v110, v41
	s_waitcnt lgkmcnt(0)
	v_mfma_f32_16x16x32_f16 v[10:13], v[42:45], v[76:79], v[10:13]
	ds_read_b128 v[42:45], v115 offset:12288
	v_exp_f32_e32 v34, v34
	v_exp_f32_e32 v36, v36
	v_mfma_f32_16x16x32_f16 v[18:21], v[102:105], v[76:79], v[18:21]
	v_exp_f32_e32 v37, v37
	v_exp_f32_e32 v35, v35
	v_mfma_f32_16x16x32_f16 v[14:17], v[116:119], v[76:79], v[14:17]
	v_cvt_pk_f16_f32 v37, v36, v37
	v_cvt_pk_f16_f32 v36, v34, v35
	v_cvt_pk_f16_f32 v35, v109, v110
	v_cvt_pk_f16_f32 v34, v106, v107
	s_mov_b64 s[38:39], 0
	ds_read_b128 v[102:105], v115 offset:10240
	v_mfma_f32_16x16x32_f16 v[26:29], v[46:49], v[34:37], v[26:29]
	ds_read_b128 v[46:49], v115 offset:14336
	s_waitcnt lgkmcnt(0)
	v_mfma_f32_16x16x32_f16 v[18:21], v[42:45], v[34:37], v[18:21]
	v_mfma_f32_16x16x32_f16 v[22:25], v[102:105], v[34:37], v[22:25]
	v_mfma_f32_16x16x32_f16 v[10:13], v[46:49], v[34:37], v[10:13]
	v_mfma_f32_16x16x32_f16 v[14:17], v[116:119], v[34:37], v[14:17]

.LBB2_7:
	s_add_i32 s37, s64, -1
	s_and_b32 s37, s37, 1
	s_lshl_b32 s37, s37, 14
	s_add_i32 s48, s40, s64
	s_add_i32 s48, s48, -1
	s_cmp_gt_u32 s48, s63
	s_cbranch_scc1 .Lattn_skip_tile
	v_or_b32_e32 v114, s37, v57
	v_or_b32_e32 v115, s37, v81
	ds_read_b128 v[34:37], v114
	ds_read_b128 v[38:41], v114 offset:2048
	ds_read_b128 v[42:45], v114 offset:4096
	ds_read_b128 v[110:113], v115 offset:2048
	ds_read_b128 v[46:49], v114 offset:6144
	s_cmp_ge_i32 s64, s62
	s_cbranch_scc1 .Lattn_no_dma
	s_xor_b32 s48, s37, 0x4000
	s_add_i32 s48, s50, s48
	s_mov_b32 m0, s48
	s_nop 0
	global_load_lds_dwordx4 v64, s[68:69]
	s_add_i32 m0, s48, 0x2000
	s_nop 0
	global_load_lds_dwordx4 v64, s[74:75]

.Lattn_skip_tile:
	s_cmp_ge_i32 s64, s62
	s_cbranch_scc1 .LBB2_6
	s_xor_b32 s48, s37, 0x4000
	s_add_i32 s48, s50, s48
	s_mov_b32 m0, s48
	s_nop 0
	global_load_lds_dwordx4 v64, s[68:69]
	s_add_i32 m0, s48, 0x2000
	s_nop 0
	global_load_lds_dwordx4 v64, s[74:75]
	s_branch .LBB2_6
